# QKV phase stagger of the XCD half raised to ~11 us (half a unit)
# speedup vs baseline: 1.0032x; 1.0022x over previous
.LBB0_225:
	s_add_u32 s4, s90, 0x300000
	s_addc_u32 s5, s91, 0
	s_cmp_lt_i32 s12, 2
	s_cselect_b64 s[0:1], -1, 0
	s_cmp_gt_i32 s13, 1
	s_cselect_b64 s[2:3], -1, 0
	s_and_b64 s[0:1], s[0:1], s[2:3]
	s_andn2_b64 vcc, exec, s[0:1]
	s_cbranch_vccnz .LBB0_301
	v_readlane_b32 s32, v254, 0
	s_nop 3
	s_bitcmp1_b32 s32, 2
	s_cbranch_scc0 .Lstag_0
	s_sleep 127
	s_sleep 127
	s_sleep 90

.LBB0_1164:
	s_cmp_lt_i32 s12, 12
	s_cselect_b64 s[0:1], -1, 0
	s_cmp_gt_u32 s13, 11
	s_cselect_b64 s[2:3], -1, 0
	s_and_b64 s[0:1], s[0:1], s[2:3]
	s_andn2_b64 vcc, exec, s[0:1]
	s_cbranch_vccnz .LBB0_1236
	v_readlane_b32 s32, v254, 0
	s_nop 3
	s_bitcmp1_b32 s32, 2
	s_cbranch_scc0 .Lstag_1
	s_sleep 127
	s_sleep 127
	s_sleep 90

.LBB0_2041:
	s_cmp_lt_i32 s12, 22
	s_cselect_b64 s[0:1], -1, 0
	s_cmp_gt_u32 s13, 21
	s_cselect_b64 s[2:3], -1, 0
	s_and_b64 s[0:1], s[0:1], s[2:3]
	s_andn2_b64 vcc, exec, s[0:1]
	s_cbranch_vccnz .LBB0_2113
	v_readlane_b32 s32, v254, 0
	s_nop 3
	s_bitcmp1_b32 s32, 2
	s_cbranch_scc0 .Lstag_2
	s_sleep 127
	s_sleep 127
	s_sleep 90

.LBB0_2920:
	s_cmp_gt_i32 s12, 39
	s_cselect_b64 s[0:1], -1, 0
	s_cmp_lt_i32 s13, 31
	s_cselect_b64 s[2:3], -1, 0
	s_or_b64 s[0:1], s[0:1], s[2:3]
	s_and_b64 vcc, exec, s[0:1]
	v_readlane_b32 s83, v254, 0
	s_cbranch_vccnz .LBB0_3660
	s_add_u32 s0, s90, 0x380000
	s_mov_b64 s[84:85], s[12:13]
	s_addc_u32 s1, s91, 0
	s_cmp_lt_i32 s84, 32
	s_cselect_b64 s[2:3], -1, 0
	s_cmp_gt_u32 s85, 31
	s_cselect_b64 s[4:5], -1, 0
	s_and_b64 s[2:3], s[2:3], s[4:5]
	v_readlane_b32 s86, v254, 50
	s_andn2_b64 vcc, exec, s[2:3]
	v_readlane_b32 s87, v254, 51
	s_cbranch_vccnz .LBB0_2997
	v_readlane_b32 s32, v254, 0
	s_nop 3
	s_bitcmp1_b32 s32, 2
	s_cbranch_scc0 .Lstag_3
	s_sleep 127
	s_sleep 127
	s_sleep 90
